# v56 + GEMM phase prologues stage K-tile 1 before waiting for K-tile 0 (vmcnt(8) instead of vmcnt(2) before the first barrier)
# speedup vs baseline: 1.0007x; 1.0007x over previous
; #define PG8_STAGE(bufoff, gbase, voff) do { _Pragma("unroll") for (int _i = 0; _i < 2; ++_i) \
;         __builtin_amdgcn_global_load_lds((const unsigned*)((const char*)(gbase) + (voff)[_i]), (PG8_LAS unsigned*)(lds + (bufoff) + ldsw + _i * 8192), 16, 0, 0); } while (0)
; #define PG8_WAIT_V(n) asm volatile("s_waitcnt vmcnt(" #n ")" ::: "memory")
; #define PG8_BAR __builtin_amdgcn_s_barrier()
; template <class Epi, class Sched, bool ALIGN_EPI = false, bool SP2 = false>
; __device__ __forceinline__ void gemm_phase(PG8_LAS unsigned char* lds, const Gemm g, const Sched& S, const Epi& E) {
;     ...
;         PG8_STAGE(PG8_SB(0, 0), cB, voffB); PG8_STAGE(PG8_SB(0, 1), cB + hstepB, voffB); PG8_STAGE(PG8_SA(0, 0), cA, voffA); PG8_STAGE(PG8_SA(0, 1), cA + hstepA, voffA);
;         if (wr == 1) PG8_BAR;
;         PG8_WAIT_V(2); PG8_BAR;
;         PG8_STAGE(PG8_SB(1, 0), cB + kstep, voffB); PG8_STAGE(PG8_SA(1, 0), cA + kstep, voffA); PG8_STAGE(PG8_SB(1, 1), cB + hstepB + kstep, voffB);
;         PG8_WAIT_V(6); PG8_BAR;
.LBB0_147:
	s_add_u32 s8, s4, 0x11000000
	s_addc_u32 s9, s5, 0
	s_lshl_b32 s11, s11, 5
	s_and_b32 s15, s11, 0x60
	s_add_i32 m0, s41, 0x18000
	v_lshl_add_u64 v[10:11], v[10:11], 0, s[64:65]
	s_lshl_b32 s14, s10, 13
	s_lshl_b32 s11, s15, 7
	global_load_lds_dwordx4 v[10:11], off
	v_lshl_add_u64 v[8:9], v[8:9], 0, s[64:65]
	s_add_i32 m0, s41, 0x1a000
	s_add_i32 s45, s41, 0x8000
	s_add_i32 s46, s41, 0xa000
	global_load_lds_dwordx4 v[8:9], off
	v_lshl_add_u64 v[4:5], v[4:5], 0, s[64:65]
	s_mov_b32 m0, s45
	s_add_u32 s12, s22, 0x40080
	global_load_lds_dwordx4 v[4:5], off
	v_lshl_add_u64 v[4:5], v[6:7], 0, s[64:65]
	s_mov_b32 m0, s46
	s_addc_u32 s13, s23, 0
	global_load_lds_dwordx4 v[4:5], off
	s_add_i32 m0, s41, 0x1c000
	v_lshl_add_u64 v[4:5], s[12:13], 0, v[136:137]
	global_load_lds_dwordx4 v[4:5], off
	v_lshl_add_u64 v[4:5], s[12:13], 0, v[132:133]
	s_add_i32 m0, s41, 0x1e000
	s_cmpk_lt_u32 s3, 0x100
	global_load_lds_dwordx4 v[4:5], off
	s_waitcnt vmcnt(8)
	s_barrier
	v_lshrrev_b32_e32 v5, 1, v12
	v_and_b32_e32 v5, 24, v5
	v_and_b32_e32 v4, 15, v12
	v_lshlrev_b32_e32 v6, 1, v5
	v_lshl_or_b32 v2, s10, 6, v4
	v_lshl_or_b32 v4, v4, 6, v6
	v_lshlrev_b32_e32 v6, 2, v12
	v_and_b32_e32 v6, 32, v6
	v_bitop3_b32 v7, v4, s14, v6 bitop3:0xde
	v_bitop3_b32 v147, v4, s11, v6 bitop3:0xde
	v_lshlrev_b32_e32 v4, 14, v13
	v_and_b32_e32 v4, 0xffff8000, v4
	v_or_b32_e32 v148, s15, v5
	v_lshl_add_u32 v4, v14, 11, v4
	v_and_b32_e32 v5, 1, v13
	v_lshl_or_b32 v4, v5, 6, v4
	v_lshl_add_u32 v140, v15, 1, v4
	v_lshlrev_b32_e32 v4, 14, v17
	v_and_b32_e32 v4, 0xffff8000, v4
	s_waitcnt vmcnt(6)
	v_lshl_add_u32 v4, v16, 11, v4
	v_and_b32_e32 v5, 1, v17
	v_lshl_or_b32 v4, v5, 6, v4
	s_sext_i32_i16 s21, s2
	s_cselect_b64 s[10:11], -1, 0
	s_ashr_i32 s47, s1, 31
	v_mov_b32_e32 v141, v3
	v_lshl_add_u32 v142, v18, 1, v4
	v_mov_b32_e32 v143, v3
	s_mov_b32 s48, 0
	v_add_u32_e32 v149, 0, v7
	s_barrier
	s_branch .LBB0_150

; #define PG8_STAGE(bufoff, gbase, voff) do { _Pragma("unroll") for (int _i = 0; _i < 2; ++_i) \
;         __builtin_amdgcn_global_load_lds((const unsigned*)((const char*)(gbase) + (voff)[_i]), (PG8_LAS unsigned*)(lds + (bufoff) + ldsw + _i * 8192), 16, 0, 0); } while (0)
; #define PG8_WAIT_V(n) asm volatile("s_waitcnt vmcnt(" #n ")" ::: "memory")
; #define PG8_BAR __builtin_amdgcn_s_barrier()
; template <class Epi, class Sched, bool ALIGN_EPI = false, bool SP2 = false>
; __device__ __forceinline__ void gemm_phase(PG8_LAS unsigned char* lds, const Gemm g, const Sched& S, const Epi& E) {
;     ...
;         PG8_STAGE(PG8_SB(0, 0), cB, voffB); PG8_STAGE(PG8_SB(0, 1), cB + hstepB, voffB); PG8_STAGE(PG8_SA(0, 0), cA, voffA); PG8_STAGE(PG8_SA(0, 1), cA + hstepA, voffA);
;         if (wr == 1) PG8_BAR;
;         PG8_WAIT_V(2); PG8_BAR;
;         PG8_STAGE(PG8_SB(1, 0), cB + kstep, voffB); PG8_STAGE(PG8_SA(1, 0), cA + kstep, voffA); PG8_STAGE(PG8_SB(1, 1), cB + hstepB + kstep, voffB);
;         PG8_WAIT_V(6); PG8_BAR;
.LBB0_655:
	v_lshrrev_b32_e32 v22, 1, v20
	v_and_b32_e32 v22, 24, v22
	s_sext_i32_i8 s43, s8
	s_add_u32 s8, s2, 0xd000000
	v_and_b32_e32 v21, 15, v20
	v_lshlrev_b32_e32 v23, 1, v22
	v_lshlrev_b32_e32 v20, 2, v20
	s_addc_u32 s9, s3, 0
	v_lshl_or_b32 v2, s5, 6, v21
	v_lshl_or_b32 v21, v21, 6, v23
	s_lshl_b32 s2, s5, 13
	v_and_b32_e32 v20, 32, v20
	v_bitop3_b32 v23, v21, s2, v20 bitop3:0xde
	s_lshl_b32 s2, s4, 5
	s_and_b32 s4, s2, 0x60
	s_add_i32 m0, s28, 0x18000
	v_lshl_add_u64 v[10:11], v[10:11], 0, s[64:65]
	s_lshl_b32 s2, s4, 7
	global_load_lds_dwordx4 v[10:11], off
	v_lshl_add_u64 v[8:9], v[8:9], 0, s[64:65]
	s_add_i32 m0, s28, 0x1a000
	s_add_i32 s33, s28, 0x8000
	s_add_i32 s34, s28, 0xa000
	v_bitop3_b32 v146, v21, s2, v20 bitop3:0xde
	global_load_lds_dwordx4 v[8:9], off
	v_lshl_add_u64 v[4:5], v[4:5], 0, s[64:65]
	s_mov_b32 m0, s33
	s_add_u32 s2, s16, 0xb0080
	global_load_lds_dwordx4 v[4:5], off
	v_lshl_add_u64 v[4:5], v[6:7], 0, s[64:65]
	s_mov_b32 m0, s34
	s_addc_u32 s3, s17, 0
	global_load_lds_dwordx4 v[4:5], off
	s_add_i32 m0, s28, 0x1c000
	v_lshl_add_u64 v[4:5], s[2:3], 0, v[134:135]
	global_load_lds_dwordx4 v[4:5], off
	v_lshl_add_u64 v[4:5], s[2:3], 0, v[138:139]
	s_add_i32 m0, s28, 0x1e000
	v_or_b32_e32 v147, s4, v22
	global_load_lds_dwordx4 v[4:5], off
	s_waitcnt vmcnt(8)
	s_barrier
	s_movk_i32 s4, 0xb00
	v_lshrrev_b32_e32 v5, 1, v16
	v_mul_lo_u32 v4, v18, s4
	s_mov_b32 s5, 0xb000
	v_mad_u64_u32 v[4:5], s[2:3], v5, s5, v[4:5]
	v_or_b32_e32 v4, v4, v17
	v_add_lshl_u32 v4, v4, v19, 1
	v_mov_b32_e32 v5, v3
	s_mov_b64 s[12:13], 0xb0080
	v_lshl_add_u64 v[140:141], v[4:5], 0, s[12:13]
	v_lshrrev_b32_e32 v5, 1, v12
	v_mul_lo_u32 v4, v14, s4
	v_mad_u64_u32 v[4:5], s[2:3], v5, s5, v[4:5]
	s_waitcnt vmcnt(6)
	v_or_b32_e32 v4, v4, v13
	s_cmpk_lt_u32 s10, 0x100
	v_add_lshl_u32 v4, v4, v15, 1
	v_mov_b32_e32 v5, v3
	s_cselect_b64 s[10:11], -1, 0
	s_ashr_i32 s35, s0, 31
	v_lshl_add_u64 v[142:143], v[4:5], 0, s[12:13]
	s_mov_b32 s39, 0
	v_add_u32_e32 v148, 0, v23
	s_barrier
	s_branch .LBB0_658

; #define PG8_STAGE(bufoff, gbase, voff) do { _Pragma("unroll") for (int _i = 0; _i < 2; ++_i) \
;         __builtin_amdgcn_global_load_lds((const unsigned*)((const char*)(gbase) + (voff)[_i]), (PG8_LAS unsigned*)(lds + (bufoff) + ldsw + _i * 8192), 16, 0, 0); } while (0)
; #define PG8_WAIT_V(n) asm volatile("s_waitcnt vmcnt(" #n ")" ::: "memory")
; #define PG8_BAR __builtin_amdgcn_s_barrier()
; template <class Epi, class Sched, bool ALIGN_EPI = false, bool SP2 = false>
; __device__ __forceinline__ void gemm_phase(PG8_LAS unsigned char* lds, const Gemm g, const Sched& S, const Epi& E) {
;     ...
;         PG8_STAGE(PG8_SB(0, 0), cB, voffB); PG8_STAGE(PG8_SB(0, 1), cB + hstepB, voffB); PG8_STAGE(PG8_SA(0, 0), cA, voffA); PG8_STAGE(PG8_SA(0, 1), cA + hstepA, voffA);
;         if (wr == 1) PG8_BAR;
;         PG8_WAIT_V(2); PG8_BAR;
;         PG8_STAGE(PG8_SB(1, 0), cB + kstep, voffB); PG8_STAGE(PG8_SA(1, 0), cA + kstep, voffA); PG8_STAGE(PG8_SB(1, 1), cB + hstepB + kstep, voffB);
;         PG8_WAIT_V(6); PG8_BAR;
.LBB0_810:
	v_lshrrev_b32_e32 v19, 1, v17
	v_and_b32_e32 v19, 24, v19
	s_add_u32 s41, s4, 0x11000000
	v_and_b32_e32 v18, 15, v17
	v_lshlrev_b32_e32 v20, 1, v19
	v_lshlrev_b32_e32 v17, 2, v17
	s_addc_u32 s42, s5, 0
	v_lshl_or_b32 v152, s17, 6, v18
	v_lshl_or_b32 v18, v18, 6, v20
	s_lshl_b32 s4, s17, 13
	v_and_b32_e32 v17, 32, v17
	v_bitop3_b32 v20, v18, s4, v17 bitop3:0xde
	s_lshl_b32 s4, s16, 5
	s_and_b32 s16, s4, 0x60
	s_add_i32 m0, s35, 0x18000
	v_lshl_add_u64 v[10:11], v[10:11], 0, s[64:65]
	s_lshl_b32 s4, s16, 7
	global_load_lds_dwordx4 v[10:11], off
	v_lshl_add_u64 v[8:9], v[8:9], 0, s[64:65]
	s_add_i32 m0, s35, 0x1a000
	s_add_i32 s43, s35, 0x8000
	s_add_i32 s44, s35, 0xa000
	v_bitop3_b32 v153, v18, s4, v17 bitop3:0xde
	global_load_lds_dwordx4 v[8:9], off
	v_lshl_add_u64 v[4:5], v[4:5], 0, s[64:65]
	s_mov_b32 m0, s43
	s_add_u32 s4, s26, 0x40080
	global_load_lds_dwordx4 v[4:5], off
	v_lshl_add_u64 v[4:5], v[6:7], 0, s[64:65]
	s_mov_b32 m0, s44
	s_addc_u32 s5, s27, 0
	global_load_lds_dwordx4 v[4:5], off
	s_add_i32 m0, s35, 0x1c000
	v_lshl_add_u64 v[4:5], s[4:5], 0, v[136:137]
	global_load_lds_dwordx4 v[4:5], off
	v_lshl_add_u64 v[4:5], s[4:5], 0, v[132:133]
	s_add_i32 m0, s35, 0x1e000
	s_cmpk_lt_u32 s15, 0x100
	global_load_lds_dwordx4 v[4:5], off
	s_waitcnt vmcnt(8)
	s_barrier
	v_lshlrev_b32_e32 v5, 14, v2
	v_and_b32_e32 v5, 0xffff8000, v5
	v_lshl_add_u32 v5, v12, 11, v5
	v_and_b32_e32 v2, 1, v2
	v_lshl_or_b32 v2, v2, 6, v5
	v_lshl_add_u32 v142, v13, 1, v2
	v_lshlrev_b32_e32 v2, 14, v15
	v_and_b32_e32 v2, 0xffff8000, v2
	s_waitcnt vmcnt(6)
	v_or_b32_e32 v4, s16, v19
	v_lshl_add_u32 v2, v14, 11, v2
	v_and_b32_e32 v5, 1, v15
	v_lshlrev_b32_e32 v6, 2, v4
	v_mov_b32_e32 v7, v3
	v_lshl_or_b32 v2, v5, 6, v2
	s_sext_i32_i8 s47, s14
	s_cselect_b64 s[14:15], -1, 0
	v_cmp_gt_u32_e64 s[4:5], 16, v4
	s_ashr_i32 s45, s0, 31
	v_lshl_add_u64 v[140:141], s[6:7], 0, v[6:7]
	v_mov_b32_e32 v143, v3
	v_lshl_add_u32 v144, v16, 1, v2
	v_mov_b32_e32 v145, v3
	s_mov_b32 s46, 0
	v_add_u32_e32 v154, 0, v20
	v_lshlrev_b32_e32 v146, 1, v4
	s_barrier
	s_branch .LBB0_813

; #define PG8_STAGE(bufoff, gbase, voff) do { _Pragma("unroll") for (int _i = 0; _i < 2; ++_i) \
;         __builtin_amdgcn_global_load_lds((const unsigned*)((const char*)(gbase) + (voff)[_i]), (PG8_LAS unsigned*)(lds + (bufoff) + ldsw + _i * 8192), 16, 0, 0); } while (0)
; #define PG8_WAIT_V(n) asm volatile("s_waitcnt vmcnt(" #n ")" ::: "memory")
; #define PG8_BAR __builtin_amdgcn_s_barrier()
; template <class Epi, class Sched, bool ALIGN_EPI = false, bool SP2 = false>
; __device__ __forceinline__ void gemm_phase(PG8_LAS unsigned char* lds, const Gemm g, const Sched& S, const Epi& E) {
;     ...
;         PG8_STAGE(PG8_SB(0, 0), cB, voffB); PG8_STAGE(PG8_SB(0, 1), cB + hstepB, voffB); PG8_STAGE(PG8_SA(0, 0), cA, voffA); PG8_STAGE(PG8_SA(0, 1), cA + hstepA, voffA);
;         if (wr == 1) PG8_BAR;
;         PG8_WAIT_V(2); PG8_BAR;
;         PG8_STAGE(PG8_SB(1, 0), cB + kstep, voffB); PG8_STAGE(PG8_SA(1, 0), cA + kstep, voffA); PG8_STAGE(PG8_SB(1, 1), cB + hstepB + kstep, voffB);
;         PG8_WAIT_V(6); PG8_BAR;
.LBB0_1083:
	v_lshrrev_b32_e32 v20, 1, v18
	v_and_b32_e32 v20, 24, v20
	s_sext_i32_i8 s43, s8
	s_add_u32 s8, s4, 0xd000000
	v_and_b32_e32 v19, 15, v18
	v_lshlrev_b32_e32 v21, 1, v20
	v_lshlrev_b32_e32 v18, 2, v18
	s_addc_u32 s9, s5, 0
	v_lshl_or_b32 v2, s12, 6, v19
	v_lshl_or_b32 v19, v19, 6, v21
	s_lshl_b32 s4, s12, 13
	v_and_b32_e32 v18, 32, v18
	v_bitop3_b32 v21, v19, s4, v18 bitop3:0xde
	s_lshl_b32 s4, s11, 5
	s_and_b32 s12, s4, 0x60
	s_add_i32 m0, s17, 0x18000
	v_lshl_add_u64 v[10:11], v[10:11], 0, s[64:65]
	s_lshl_b32 s4, s12, 7
	global_load_lds_dwordx4 v[10:11], off
	v_lshl_add_u64 v[8:9], v[8:9], 0, s[64:65]
	s_add_i32 m0, s17, 0x1a000
	s_add_i32 s39, s17, 0x8000
	s_add_i32 s40, s17, 0xa000
	v_bitop3_b32 v146, v19, s4, v18 bitop3:0xde
	global_load_lds_dwordx4 v[8:9], off
	v_lshl_add_u64 v[4:5], v[4:5], 0, s[64:65]
	s_mov_b32 m0, s39
	s_add_u32 s4, s22, 0x40080
	global_load_lds_dwordx4 v[4:5], off
	v_lshl_add_u64 v[4:5], v[6:7], 0, s[64:65]
	s_mov_b32 m0, s40
	s_addc_u32 s5, s23, 0
	global_load_lds_dwordx4 v[4:5], off
	s_add_i32 m0, s17, 0x1c000
	v_lshl_add_u64 v[4:5], s[4:5], 0, v[134:135]
	global_load_lds_dwordx4 v[4:5], off
	v_lshl_add_u64 v[4:5], s[4:5], 0, v[138:139]
	s_add_i32 m0, s17, 0x1e000
	s_cmpk_lt_u32 s10, 0x100
	global_load_lds_dwordx4 v[4:5], off
	s_waitcnt vmcnt(8)
	s_barrier
	v_lshlrev_b32_e32 v4, 14, v15
	v_and_b32_e32 v4, 0xffff8000, v4
	v_lshl_add_u32 v4, v16, 11, v4
	v_and_b32_e32 v5, 1, v15
	v_lshl_or_b32 v4, v5, 6, v4
	v_lshl_add_u32 v140, v17, 1, v4
	v_lshlrev_b32_e32 v4, 14, v12
	v_and_b32_e32 v4, 0xffff8000, v4
	s_waitcnt vmcnt(6)
	v_lshl_add_u32 v4, v13, 11, v4
	v_and_b32_e32 v5, 1, v12
	v_lshl_or_b32 v4, v5, 6, v4
	s_cselect_b64 s[10:11], -1, 0
	s_ashr_i32 s41, s0, 31
	v_or_b32_e32 v147, s12, v20
	v_mov_b32_e32 v141, v3
	v_lshl_add_u32 v142, v14, 1, v4
	v_mov_b32_e32 v143, v3
	s_mov_b32 s42, 0
	v_add_u32_e32 v148, 0, v21
	s_barrier
	s_branch .LBB0_1086

; #define PG8_STAGE(bufoff, gbase, voff) do { _Pragma("unroll") for (int _i = 0; _i < 2; ++_i) \
;         __builtin_amdgcn_global_load_lds((const unsigned*)((const char*)(gbase) + (voff)[_i]), (PG8_LAS unsigned*)(lds + (bufoff) + ldsw + _i * 8192), 16, 0, 0); } while (0)
; #define PG8_WAIT_V(n) asm volatile("s_waitcnt vmcnt(" #n ")" ::: "memory")
; #define PG8_BAR __builtin_amdgcn_s_barrier()
; template <class Epi, class Sched, bool ALIGN_EPI = false, bool SP2 = false>
; __device__ __forceinline__ void gemm_phase(PG8_LAS unsigned char* lds, const Gemm g, const Sched& S, const Epi& E) {
;     ...
;         PG8_STAGE(PG8_SB(0, 0), cB, voffB); PG8_STAGE(PG8_SB(0, 1), cB + hstepB, voffB); PG8_STAGE(PG8_SA(0, 0), cA, voffA); PG8_STAGE(PG8_SA(0, 1), cA + hstepA, voffA);
;         if (wr == 1) PG8_BAR;
;         PG8_WAIT_V(2); PG8_BAR;
;         PG8_STAGE(PG8_SB(1, 0), cB + kstep, voffB); PG8_STAGE(PG8_SA(1, 0), cA + kstep, voffA); PG8_STAGE(PG8_SB(1, 1), cB + hstepB + kstep, voffB);
;         PG8_WAIT_V(6); PG8_BAR;
.LBB0_1157:
	v_lshrrev_b32_e32 v19, 1, v16
	v_and_b32_e32 v19, 24, v19
	s_add_u32 s10, s14, 0x11000000
	v_and_b32_e32 v2, 15, v16
	v_lshlrev_b32_e32 v20, 1, v19
	v_lshlrev_b32_e32 v16, 2, v16
	s_addc_u32 s11, s15, 0
	s_and_b32 s3, s23, 3
	s_lshl_b32 s37, s2, 6
	v_lshl_or_b32 v20, v2, 6, v20
	s_lshl_b32 s2, s2, 13
	v_and_b32_e32 v16, 32, v16
	s_add_i32 m0, s31, 0x18000
	v_lshl_add_u64 v[10:11], v[10:11], 0, s[64:65]
	v_bitop3_b32 v21, v20, s2, v16 bitop3:0xde
	s_lshl_b32 s19, s3, 5
	s_lshl_b32 s2, s3, 12
	global_load_lds_dwordx4 v[10:11], off
	v_lshl_add_u64 v[8:9], v[8:9], 0, s[64:65]
	s_add_i32 m0, s31, 0x1a000
	s_add_i32 s38, s31, 0x8000
	s_add_i32 s39, s31, 0xa000
	v_bitop3_b32 v154, v20, s2, v16 bitop3:0xde
	global_load_lds_dwordx4 v[8:9], off
	v_lshl_add_u64 v[4:5], v[4:5], 0, s[64:65]
	s_mov_b32 m0, s38
	s_add_u32 s2, s4, 0x40080
	global_load_lds_dwordx4 v[4:5], off
	v_lshl_add_u64 v[4:5], v[6:7], 0, s[64:65]
	s_mov_b32 m0, s39
	s_addc_u32 s3, s5, 0
	global_load_lds_dwordx4 v[4:5], off
	s_add_i32 m0, s31, 0x1c000
	v_lshl_add_u64 v[4:5], s[2:3], 0, v[134:135]
	global_load_lds_dwordx4 v[4:5], off
	v_lshl_add_u64 v[4:5], s[2:3], 0, v[138:139]
	s_add_i32 m0, s31, 0x1e000
	v_mov_b32_e32 v7, v3
	global_load_lds_dwordx4 v[4:5], off
	s_waitcnt vmcnt(8)
	s_barrier
	v_or_b32_e32 v4, s19, v19
	v_lshlrev_b32_e32 v6, 2, v4
	v_bitop3_b32 v5, s19, 56, v19 bitop3:0xc8
	v_lshl_add_u64 v[6:7], s[14:15], 0, v[6:7]
	s_mov_b64 s[24:25], 0x400000
	v_lshl_add_u64 v[140:141], v[6:7], 0, s[24:25]
	v_lshlrev_b32_e32 v6, 1, v5
	v_mov_b32_e32 v7, v3
	v_lshlrev_b32_e32 v5, 14, v15
	s_cmpk_lt_u32 s12, 0x100
	v_lshl_add_u64 v[6:7], s[14:15], 0, v[6:7]
	s_mov_b64 s[14:15], 0x13000000
	v_and_b32_e32 v5, 0xffff8000, v5
	s_cselect_b64 s[12:13], -1, 0
	v_lshl_add_u64 v[142:143], v[6:7], 0, s[14:15]
	s_lshl_b32 s15, s17, 3
	s_bfe_u32 s17, s16, 0x30003
	v_lshl_add_u32 v5, v17, 11, v5
	v_and_b32_e32 v6, 1, v15
	s_add_i32 s22, s22, 16
	s_or_b32 s42, s15, s17
	s_lshr_b32 s15, s16, 6
	v_lshl_or_b32 v5, v6, 6, v5
	s_lshr_b32 s14, s22, 3
	s_and_b32 s15, s15, 2
	v_lshl_add_u32 v144, v18, 1, v5
	v_lshlrev_b32_e32 v5, 14, v12
	s_add_i32 s43, s14, s15
	v_readlane_b32 s14, v253, 57
	v_and_b32_e32 v5, 0xffff8000, v5
	s_waitcnt vmcnt(6)
	s_mov_b32 s16, s14
	s_mov_b32 s17, s14
	v_lshl_add_u32 v5, v13, 11, v5
	v_and_b32_e32 v6, 1, v12
	s_bfe_u32 s40, s23, 0x10001
	v_readlane_b32 s15, v253, 58
	v_writelane_b32 v253, s16, 57
	v_lshl_or_b32 v5, v6, 6, v5
	v_cmp_gt_u32_e64 s[2:3], 48, v4
	s_or_b32 s41, s40, 2
	v_writelane_b32 v253, s17, 58
	s_mov_b32 s15, s16
	v_mov_b32_e32 v145, v3
	v_lshl_add_u32 v146, v14, 1, v5
	v_mov_b32_e32 v147, v3
	s_mov_b64 s[16:17], -1
	v_add_u32_e32 v155, 0, v21
	v_lshlrev_b32_e32 v148, 1, v4
	s_barrier
	s_branch .LBB0_1160

; #define PG8_STAGE(bufoff, gbase, voff) do { _Pragma("unroll") for (int _i = 0; _i < 2; ++_i) \
;         __builtin_amdgcn_global_load_lds((const unsigned*)((const char*)(gbase) + (voff)[_i]), (PG8_LAS unsigned*)(lds + (bufoff) + ldsw + _i * 8192), 16, 0, 0); } while (0)
; #define PG8_WAIT_V(n) asm volatile("s_waitcnt vmcnt(" #n ")" ::: "memory")
; #define PG8_BAR __builtin_amdgcn_s_barrier()
; template <class Epi, class Sched, bool ALIGN_EPI = false, bool SP2 = false>
; __device__ __forceinline__ void gemm_phase(PG8_LAS unsigned char* lds, const Gemm g, const Sched& S, const Epi& E) {
;     ...
;         PG8_STAGE(PG8_SB(0, 0), cB, voffB); PG8_STAGE(PG8_SB(0, 1), cB + hstepB, voffB); PG8_STAGE(PG8_SA(0, 0), cA, voffA); PG8_STAGE(PG8_SA(0, 1), cA + hstepA, voffA);
;         if (wr == 1) PG8_BAR;
;         PG8_WAIT_V(2); PG8_BAR;
;         PG8_STAGE(PG8_SB(1, 0), cB + kstep, voffB); PG8_STAGE(PG8_SA(1, 0), cA + kstep, voffA); PG8_STAGE(PG8_SB(1, 1), cB + hstepB + kstep, voffB);
;         PG8_WAIT_V(6); PG8_BAR;
.LBB0_1231:
	s_lshl_b64 s[12:13], s[68:69], 22
	s_add_u32 s12, s2, s12
	v_lshrrev_b32_e32 v20, 1, v18
	s_addc_u32 s13, s3, s13
	s_ashr_i32 s14, s8, 31
	v_and_b32_e32 v20, 24, v20
	s_lshl_b32 s9, s9, 5
	v_and_b32_e32 v19, 15, v18
	s_lshr_b32 s14, s14, 26
	v_lshlrev_b32_e32 v21, 1, v20
	s_and_b32 s18, s9, 0x60
	v_lshlrev_b32_e32 v18, 2, v18
	s_add_i32 s14, s8, s14
	v_lshl_or_b32 v2, s11, 6, v19
	v_lshl_or_b32 v19, v19, 6, v21
	s_lshl_b32 s9, s18, 7
	v_and_b32_e32 v18, 32, v18
	s_add_i32 m0, s28, 0x18000
	v_lshl_add_u64 v[10:11], v[10:11], 0, s[64:65]
	s_ashr_i32 s33, s14, 6
	v_bitop3_b32 v146, v19, s9, v18 bitop3:0xde
	s_lshl_b32 s9, s11, 13
	global_load_lds_dwordx4 v[10:11], off
	v_lshl_add_u64 v[8:9], v[8:9], 0, s[64:65]
	s_add_i32 m0, s28, 0x1a000
	s_add_i32 s34, s28, 0x8000
	s_add_i32 s35, s28, 0xa000
	global_load_lds_dwordx4 v[8:9], off
	v_lshl_add_u64 v[4:5], v[4:5], 0, s[64:65]
	s_mov_b32 m0, s34
	s_add_u32 s14, s4, 0x80080
	global_load_lds_dwordx4 v[4:5], off
	v_lshl_add_u64 v[4:5], v[6:7], 0, s[64:65]
	s_mov_b32 m0, s35
	s_addc_u32 s15, s5, 0
	global_load_lds_dwordx4 v[4:5], off
	s_add_i32 m0, s28, 0x1c000
	v_lshl_add_u64 v[4:5], s[14:15], 0, v[134:135]
	global_load_lds_dwordx4 v[4:5], off
	v_lshl_add_u64 v[4:5], s[14:15], 0, v[138:139]
	s_add_i32 m0, s28, 0x1e000
	s_cmp_gt_i32 s8, 63
	global_load_lds_dwordx4 v[4:5], off
	s_waitcnt vmcnt(8)
	s_barrier
	v_or_b32_e32 v4, s18, v20
	v_lshlrev_b32_e32 v4, 1, v4
	v_mov_b32_e32 v5, v3
	v_lshl_add_u64 v[4:5], s[12:13], 0, v[4:5]
	s_mov_b64 s[12:13], 0xd000000
	v_lshl_add_u64 v[140:141], v[4:5], 0, s[12:13]
	v_lshlrev_b32_e32 v4, 14, v15
	v_and_b32_e32 v4, 0xffff8000, v4
	v_lshl_add_u32 v4, v16, 11, v4
	v_and_b32_e32 v5, 1, v15
	v_lshl_or_b32 v4, v5, 6, v4
	v_lshl_add_u32 v142, v17, 1, v4
	v_lshlrev_b32_e32 v4, 14, v12
	v_and_b32_e32 v4, 0xffff8000, v4
	v_bitop3_b32 v18, v19, s9, v18 bitop3:0xde
	s_waitcnt vmcnt(6)
	s_cselect_b64 s[8:9], -1, 0
	s_add_i32 s37, s33, -2
	v_lshl_add_u32 v4, v13, 11, v4
	v_and_b32_e32 v5, 1, v12
	s_cmpk_lt_u32 s10, 0x100
	v_lshl_or_b32 v4, v5, 6, v4
	s_cselect_b64 s[10:11], -1, 0
	v_mov_b32_e32 v143, v3
	v_lshl_add_u32 v144, v14, 1, v4
	v_mov_b32_e32 v145, v3
	s_mov_b32 s41, 0
	v_add_u32_e32 v147, 0, v18
	s_mov_b32 s42, s27
	s_mov_b64 s[18:19], s[4:5]
	s_barrier
	s_branch .LBB0_1234

; #define PG8_STAGE(bufoff, gbase, voff) do { _Pragma("unroll") for (int _i = 0; _i < 2; ++_i) \
;         __builtin_amdgcn_global_load_lds((const unsigned*)((const char*)(gbase) + (voff)[_i]), (PG8_LAS unsigned*)(lds + (bufoff) + ldsw + _i * 8192), 16, 0, 0); } while (0)
; #define PG8_WAIT_V(n) asm volatile("s_waitcnt vmcnt(" #n ")" ::: "memory")
; #define PG8_BAR __builtin_amdgcn_s_barrier()
; template <class Epi, class Sched, bool ALIGN_EPI = false, bool SP2 = false>
; __device__ __forceinline__ void gemm_phase(PG8_LAS unsigned char* lds, const Gemm g, const Sched& S, const Epi& E) {
;     ...
;     f32x4 acc[2][2][4][2];
; #pragma unroll
;     for (int a = 0; a < 2; ++a)
; #pragma unroll
;         for (int b = 0; b < 2; ++b)
; #pragma unroll
;             for (int m = 0; m < 4; ++m)
; #pragma unroll
;                 for (int n = 0; n < 2; ++n) acc[a][b][m][n] = (f32x4){0.f, 0.f, 0.f, 0.f};
;     ...
;         PG8_STAGE(PG8_SB(0, 0), cB, voffB); PG8_STAGE(PG8_SB(0, 1), cB + hstepB, voffB); PG8_STAGE(PG8_SA(0, 0), cA, voffA); PG8_STAGE(PG8_SA(0, 1), cA + hstepA, voffA);
;         if (wr == 1) PG8_BAR;
;         PG8_WAIT_V(2); PG8_BAR;
;         PG8_STAGE(PG8_SB(1, 0), cB + kstep, voffB); PG8_STAGE(PG8_SA(1, 0), cA + kstep, voffA); PG8_STAGE(PG8_SB(1, 1), cB + hstepB + kstep, voffB);
;         PG8_WAIT_V(6); PG8_BAR;
.LBB0_1246:
	v_lshrrev_b32_e32 v15, 1, v14
	v_and_b32_e32 v144, 24, v15
	v_and_b32_e32 v2, 15, v14
	v_lshlrev_b32_e32 v15, 1, v144
	v_lshlrev_b32_e32 v14, 2, v14
	s_and_b32 s15, s8, 3
	v_lshl_or_b32 v15, v2, 6, v15
	s_lshl_b32 s8, s13, 13
	v_and_b32_e32 v14, 32, v14
	v_readlane_b32 s28, v253, 55
	v_bitop3_b32 v16, v15, s8, v14 bitop3:0xde
	s_lshl_b32 s8, s15, 12
	v_readlane_b32 s29, v253, 56
	v_bitop3_b32 v145, v15, s8, v14 bitop3:0xde
	s_lshr_b64 s[26:27], s[28:29], 2
	s_lshr_b32 s8, s29, 2
	s_lshl_b32 s25, s13, 6
	s_mul_i32 s8, s8, 0x580000
	s_mul_hi_u32 s13, s26, 0x580000
	s_add_i32 s13, s13, s8
	s_mul_i32 s8, s26, 0x580000
	s_add_u32 s26, s11, 0x8d00080
	v_mov_b32_e32 v135, v3
	s_addc_u32 s27, s12, 0
	v_mov_b32_e32 v139, v3
	s_add_i32 m0, s19, 0x18000
	v_lshl_add_u64 v[14:15], s[26:27], 0, v[134:135]
	global_load_lds_dwordx4 v[14:15], off
	v_lshl_add_u64 v[14:15], s[26:27], 0, v[138:139]
	s_add_i32 m0, s19, 0x1a000
	s_add_i32 s26, s19, 0x8000
	s_add_i32 s27, s19, 0xa000
	global_load_lds_dwordx4 v[14:15], off
	v_lshl_add_u64 v[6:7], v[6:7], 0, s[64:65]
	s_mov_b32 m0, s26
	s_add_u32 s28, s11, 0x8d40080
	global_load_lds_dwordx4 v[6:7], off
	v_lshl_add_u64 v[4:5], v[4:5], 0, s[64:65]
	s_mov_b32 m0, s27
	s_addc_u32 s29, s12, 0
	global_load_lds_dwordx4 v[4:5], off
	s_add_i32 m0, s19, 0x1c000
	v_lshl_add_u64 v[4:5], s[28:29], 0, v[134:135]
	global_load_lds_dwordx4 v[4:5], off
	v_lshl_add_u64 v[4:5], s[28:29], 0, v[138:139]
	s_add_i32 m0, s19, 0x1e000
	s_add_u32 s8, s8, s10
	global_load_lds_dwordx4 v[4:5], off
	s_waitcnt vmcnt(8)
	s_barrier
	s_addc_u32 s10, s13, 0
	s_add_u32 s8, s2, s8
	s_addc_u32 s10, s3, s10
	s_add_u32 s28, s8, 0x8d00100
	s_addc_u32 s29, s10, 0
	s_and_b32 s8, s23, 7
	s_lshl_b32 s8, s8, 22
	s_lshl_b32 s9, s9, 19
	v_lshlrev_b32_e32 v4, 14, v11
	s_or_b32 s8, s8, s9
	v_and_b32_e32 v4, 0xffff8000, v4
	s_add_u32 s23, s2, s8
	v_lshl_add_u32 v4, v12, 11, v4
	v_and_b32_e32 v5, 1, v11
	s_addc_u32 s30, s3, 0
	v_lshl_or_b32 v4, v5, 6, v4
	s_add_u32 s8, s23, 0xb040080
	v_lshl_add_u32 v4, v13, 1, v4
	v_mov_b32_e32 v5, v3
	s_addc_u32 s9, s30, 0
	v_lshl_add_u64 v[140:141], s[8:9], 0, v[4:5]
	v_lshlrev_b32_e32 v4, 14, v8
	v_and_b32_e32 v4, 0xffff8000, v4
	v_lshl_add_u32 v4, v9, 11, v4
	v_and_b32_e32 v5, 1, v8
	v_lshl_or_b32 v4, v5, 6, v4
	s_waitcnt vmcnt(6)
	v_lshl_add_u32 v4, v10, 1, v4
	v_mov_b32_e32 v5, v3
	v_lshl_add_u64 v[142:143], s[8:9], 0, v[4:5]
	v_mov_b32_e32 v4, 0
	s_mov_b32 s31, -2
	s_mov_b64 s[8:9], 0
	v_add_u32_e32 v146, 0, v16
	v_mov_b32_e32 v5, v4
	v_mov_b32_e32 v6, v4
	v_mov_b32_e32 v7, v4
	v_mov_b32_e32 v8, v4
	v_mov_b32_e32 v9, v4
	v_mov_b32_e32 v10, v4
	v_mov_b32_e32 v11, v4
	v_mov_b32_e32 v12, v4
	v_mov_b32_e32 v13, v4
	v_mov_b32_e32 v14, v4
	v_mov_b32_e32 v15, v4
	v_mov_b32_e32 v20, v4
	v_mov_b32_e32 v21, v4
	v_mov_b32_e32 v22, v4
	v_mov_b32_e32 v23, v4
	v_mov_b32_e32 v28, v4
	v_mov_b32_e32 v29, v4
	v_mov_b32_e32 v30, v4
	v_mov_b32_e32 v31, v4
	v_mov_b32_e32 v36, v4
	v_mov_b32_e32 v37, v4
	v_mov_b32_e32 v38, v4
	v_mov_b32_e32 v39, v4
	v_mov_b32_e32 v48, v4
	v_mov_b32_e32 v49, v4
	v_mov_b32_e32 v50, v4
	v_mov_b32_e32 v51, v4
	v_mov_b32_e32 v56, v4
	v_mov_b32_e32 v57, v4
	v_mov_b32_e32 v58, v4
	v_mov_b32_e32 v59, v4
	v_mov_b32_e32 v16, v4
	v_mov_b32_e32 v17, v4
	v_mov_b32_e32 v18, v4
	v_mov_b32_e32 v19, v4
	v_mov_b32_e32 v24, v4
	v_mov_b32_e32 v25, v4
	v_mov_b32_e32 v26, v4
	v_mov_b32_e32 v27, v4
	v_mov_b32_e32 v32, v4
	v_mov_b32_e32 v33, v4
	v_mov_b32_e32 v34, v4
	v_mov_b32_e32 v35, v4
	v_mov_b32_e32 v40, v4
	v_mov_b32_e32 v41, v4
	v_mov_b32_e32 v42, v4
	v_mov_b32_e32 v43, v4
	v_mov_b32_e32 v44, v4
	v_mov_b32_e32 v45, v4
	v_mov_b32_e32 v46, v4
	v_mov_b32_e32 v47, v4
	v_mov_b32_e32 v52, v4
	v_mov_b32_e32 v53, v4
	v_mov_b32_e32 v54, v4
	v_mov_b32_e32 v55, v4
	v_mov_b32_e32 v60, v4
	v_mov_b32_e32 v61, v4
	v_mov_b32_e32 v62, v4
	v_mov_b32_e32 v63, v4
	v_mov_b32_e32 v64, v4
	v_mov_b32_e32 v65, v4
	v_mov_b32_e32 v66, v4
	v_mov_b32_e32 v67, v4
	v_mov_b32_e32 v68, v4
	v_mov_b32_e32 v69, v4
	v_mov_b32_e32 v70, v4
	v_mov_b32_e32 v71, v4
	v_mov_b32_e32 v72, v4
	v_mov_b32_e32 v73, v4
	v_mov_b32_e32 v74, v4
	v_mov_b32_e32 v75, v4
	v_mov_b32_e32 v76, v4
	v_mov_b32_e32 v77, v4
	v_mov_b32_e32 v78, v4
	v_mov_b32_e32 v79, v4
	v_mov_b32_e32 v84, v4
	v_mov_b32_e32 v85, v4
	v_mov_b32_e32 v86, v4
	v_mov_b32_e32 v87, v4
	v_mov_b32_e32 v92, v4
	v_mov_b32_e32 v93, v4
	v_mov_b32_e32 v94, v4
	v_mov_b32_e32 v95, v4
	v_mov_b32_e32 v100, v4
	v_mov_b32_e32 v101, v4
	v_mov_b32_e32 v102, v4
	v_mov_b32_e32 v103, v4
	v_mov_b32_e32 v112, v4
	v_mov_b32_e32 v113, v4
	v_mov_b32_e32 v114, v4
	v_mov_b32_e32 v115, v4
	v_mov_b32_e32 v120, v4
	v_mov_b32_e32 v121, v4
	v_mov_b32_e32 v122, v4
	v_mov_b32_e32 v123, v4
	v_mov_b32_e32 v80, v4
	v_mov_b32_e32 v81, v4
	v_mov_b32_e32 v82, v4
	v_mov_b32_e32 v83, v4
	v_mov_b32_e32 v88, v4
	v_mov_b32_e32 v89, v4
	v_mov_b32_e32 v90, v4
	v_mov_b32_e32 v91, v4
	v_mov_b32_e32 v96, v4
	v_mov_b32_e32 v97, v4
	v_mov_b32_e32 v98, v4
	v_mov_b32_e32 v99, v4
	v_mov_b32_e32 v104, v4
	v_mov_b32_e32 v105, v4
	v_mov_b32_e32 v106, v4
	v_mov_b32_e32 v107, v4
	v_mov_b32_e32 v108, v4
	v_mov_b32_e32 v109, v4
	v_mov_b32_e32 v110, v4
	v_mov_b32_e32 v111, v4
	v_mov_b32_e32 v116, v4
	v_mov_b32_e32 v117, v4
	v_mov_b32_e32 v118, v4
	v_mov_b32_e32 v119, v4
	v_mov_b32_e32 v124, v4
	v_mov_b32_e32 v125, v4
	v_mov_b32_e32 v126, v4
	v_mov_b32_e32 v127, v4
	v_mov_b32_e32 v128, v4
	v_mov_b32_e32 v129, v4
	v_mov_b32_e32 v130, v4
	v_mov_b32_e32 v131, v4
	s_barrier

; #define PG8_STAGE(bufoff, gbase, voff) do { _Pragma("unroll") for (int _i = 0; _i < 2; ++_i) \
;         __builtin_amdgcn_global_load_lds((const unsigned*)((const char*)(gbase) + (voff)[_i]), (PG8_LAS unsigned*)(lds + (bufoff) + ldsw + _i * 8192), 16, 0, 0); } while (0)
; #define PG8_WAIT_V(n) asm volatile("s_waitcnt vmcnt(" #n ")" ::: "memory")
; #define PG8_BAR __builtin_amdgcn_s_barrier()
; template <class Epi, class Sched, bool ALIGN_EPI = false, bool SP2 = false>
; __device__ __forceinline__ void gemm_phase(PG8_LAS unsigned char* lds, const Gemm g, const Sched& S, const Epi& E) {
;     ...
;         PG8_STAGE(PG8_SB(0, 0), cB, voffB); PG8_STAGE(PG8_SB(0, 1), cB + hstepB, voffB); PG8_STAGE(PG8_SA(0, 0), cA, voffA); PG8_STAGE(PG8_SA(0, 1), cA + hstepA, voffA);
;         if (wr == 1) PG8_BAR;
;         PG8_WAIT_V(2); PG8_BAR;
;         PG8_STAGE(PG8_SB(1, 0), cB + kstep, voffB); PG8_STAGE(PG8_SA(1, 0), cA + kstep, voffA); PG8_STAGE(PG8_SB(1, 1), cB + hstepB + kstep, voffB);
;         PG8_WAIT_V(6); PG8_BAR;
.LBB0_1683:
	v_lshrrev_b32_e32 v20, 1, v18
	v_and_b32_e32 v20, 24, v20
	s_sext_i32_i8 s40, s6
	s_add_u32 s6, s2, 0xd000000
	v_and_b32_e32 v19, 15, v18
	v_lshlrev_b32_e32 v21, 1, v20
	v_lshlrev_b32_e32 v18, 2, v18
	s_addc_u32 s7, s3, 0
	v_lshl_or_b32 v2, s10, 6, v19
	v_lshl_or_b32 v19, v19, 6, v21
	s_lshl_b32 s2, s10, 13
	v_and_b32_e32 v18, 32, v18
	v_bitop3_b32 v21, v19, s2, v18 bitop3:0xde
	s_lshl_b32 s2, s9, 5
	s_and_b32 s10, s2, 0x60
	s_add_i32 m0, s15, 0x18000
	v_lshl_add_u64 v[10:11], v[10:11], 0, s[64:65]
	s_lshl_b32 s2, s10, 7
	global_load_lds_dwordx4 v[10:11], off
	v_lshl_add_u64 v[8:9], v[8:9], 0, s[64:65]
	s_add_i32 m0, s15, 0x1a000
	s_add_i32 s36, s15, 0x8000
	s_add_i32 s37, s15, 0xa000
	v_bitop3_b32 v146, v19, s2, v18 bitop3:0xde
	global_load_lds_dwordx4 v[8:9], off
	v_lshl_add_u64 v[4:5], v[4:5], 0, s[64:65]
	s_mov_b32 m0, s36
	s_add_u32 s2, s20, 0x40080
	global_load_lds_dwordx4 v[4:5], off
	v_lshl_add_u64 v[4:5], v[6:7], 0, s[64:65]
	s_mov_b32 m0, s37
	s_addc_u32 s3, s21, 0
	global_load_lds_dwordx4 v[4:5], off
	s_add_i32 m0, s15, 0x1c000
	v_lshl_add_u64 v[4:5], s[2:3], 0, v[134:135]
	global_load_lds_dwordx4 v[4:5], off
	v_lshl_add_u64 v[4:5], s[2:3], 0, v[138:139]
	s_add_i32 m0, s15, 0x1e000
	s_cmpk_lt_u32 s8, 0x100
	global_load_lds_dwordx4 v[4:5], off
	s_waitcnt vmcnt(8)
	s_barrier
	v_lshlrev_b32_e32 v4, 14, v15
	v_and_b32_e32 v4, 0xffff8000, v4
	v_lshl_add_u32 v4, v16, 11, v4
	v_and_b32_e32 v5, 1, v15
	v_lshl_or_b32 v4, v5, 6, v4
	v_lshl_add_u32 v140, v17, 1, v4
	v_lshlrev_b32_e32 v4, 14, v12
	v_and_b32_e32 v4, 0xffff8000, v4
	s_waitcnt vmcnt(6)
	v_lshl_add_u32 v4, v13, 11, v4
	v_and_b32_e32 v5, 1, v12
	v_lshl_or_b32 v4, v5, 6, v4
	s_cselect_b64 s[8:9], -1, 0
	s_ashr_i32 s38, s0, 31
	v_or_b32_e32 v147, s10, v20
	v_mov_b32_e32 v141, v3
	v_lshl_add_u32 v142, v14, 1, v4
	v_mov_b32_e32 v143, v3
	s_mov_b32 s39, 0
	v_add_u32_e32 v148, 0, v21
	s_barrier
	s_branch .LBB0_1686
